# baseline (speedup 1.0000x reference)
.LBB1_38:
	global_load_dwordx2 v[140:141], v228, s[52:53] sc1
	global_load_dwordx2 v[142:143], v228, s[52:53] offset:128 sc1
	global_load_dwordx2 v[144:145], v229, s[52:53] sc1
	global_load_dwordx2 v[148:149], v229, s[52:53] offset:128 sc1
	global_load_dwordx2 v[146:147], v230, s[52:53] sc1
	global_load_dwordx2 v[150:151], v230, s[52:53] offset:128 sc1
	s_waitcnt vmcnt(5)
	v_cmp_eq_u32_e32 vcc, s44, v141
	s_waitcnt vmcnt(4)
	v_cmp_eq_u32_e64 s[6:7], s44, v143
	s_waitcnt vmcnt(3)
	v_cmp_eq_u32_e64 s[8:9], s44, v145
	s_and_b64 s[6:7], vcc, s[6:7]
	s_waitcnt vmcnt(2)
	v_cmp_eq_u32_e64 s[10:11], s44, v149
	s_and_b64 s[6:7], s[6:7], s[8:9]
	s_waitcnt vmcnt(1)
	v_cmp_eq_u32_e64 s[12:13], s44, v147
	s_and_b64 s[6:7], s[6:7], s[10:11]
	s_waitcnt vmcnt(0)
	v_cmp_eq_u32_e64 s[14:15], s44, v151
	s_and_b64 s[6:7], s[6:7], s[12:13]
	s_and_b64 s[6:7], s[6:7], s[14:15]
	s_cmp_eq_u64 s[6:7], exec
	s_cbranch_scc1 .Lp8_got
	s_mov_b64 s[6:7], -1
	s_mov_b64 s[8:9], -1
	s_and_b32 s6, s45, 0x3ff
	s_cmpk_eq_i32 s6, 0x3ff
	s_mov_b64 s[6:7], -1
	s_mov_b64 s[10:11], -1
	s_cbranch_scc0 .LBB1_42
	s_mov_b64 s[6:7], 0
	s_cmp_lt_u32 s45, 0x80001
	s_mov_b64 s[10:11], 0
	s_cbranch_scc0 .LBB1_42
	global_load_dword v141, v167, s[22:23] offset:4 sc1
	s_waitcnt vmcnt(0)
	v_cmp_eq_u32_e64 s[10:11], 0, v141

.Lp8_got:
	s_mov_b64 s[10:11], 0
	s_branch .LBB1_47
